# v41_xpf
# baseline (speedup 1.0000x reference)
.LBB3_4:
	s_ashr_i32 s20, s3, 31
	s_mov_b32 s50, 0
	s_lshr_b32 s20, s20, 26
	s_add_i32 s20, s3, s20
	s_ashr_i32 s51, s50, 31
	s_ashr_i32 s94, s20, 6
	s_lshl_b64 s[56:57], s[50:51], 1
	s_add_u32 s20, s36, s56
	s_addc_u32 s21, s37, s57
	s_add_u32 s56, s30, s56
	s_addc_u32 s57, s31, s57
	v_lshl_add_u64 v[18:19], s[56:57], 0, v[108:109]
	v_add_co_u32_e32 v2, vcc, s35, v18
	s_nop 1
	v_addc_co_u32_e32 v3, vcc, 0, v19, vcc
	v_add_co_u32_e32 v4, vcc, s41, v18
	s_barrier
	s_nop 0
	v_addc_co_u32_e32 v5, vcc, 0, v19, vcc
	s_mul_i32 s95, s94, 0x50
	s_mul_i32 s58, s94, 0xffe9a800
	s_add_i32 s58, s58, s29
	s_cmp_gt_i32 s3, 63
	s_cbranch_scc1 .Lmy_k2_gcopy
	v_add_u32_e32 v42, s95, v1
	v_max_i32_e32 v42, 3, v42
	v_add_u32_e32 v42, -3, v42
	v_add_u32_e32 v44, s95, v112
	v_min_u32_e32 v66, 0x400, v42
	v_add_u32_e32 v42, s58, v133
	v_max_i32_e32 v44, 3, v44
	v_ashrrev_i32_e32 v43, 31, v42
	v_add_u32_e32 v44, -3, v44
	v_lshl_add_u64 v[42:43], v[66:67], 0, v[42:43]
	v_min_u32_e32 v66, 0x400, v44
	v_add_u32_e32 v44, s58, v132
	v_ashrrev_i32_e32 v45, 31, v44
	v_lshl_add_u64 v[42:43], v[42:43], 4, s[20:21]
	v_lshl_add_u64 v[44:45], v[66:67], 0, v[44:45]
	v_lshl_add_u64 v[44:45], v[44:45], 4, s[20:21]
	global_load_dwordx4 v[62:65], v[42:43], off
	global_load_dwordx4 v[58:61], v[44:45], off
	v_add_u32_e32 v42, s95, v113
	v_max_i32_e32 v42, 3, v42
	v_add_u32_e32 v42, -3, v42
	v_add_u32_e32 v44, s95, v114
	v_min_u32_e32 v66, 0x400, v42
	v_add_u32_e32 v42, s58, v131
	v_max_i32_e32 v44, 3, v44
	v_ashrrev_i32_e32 v43, 31, v42
	v_add_u32_e32 v44, -3, v44
	v_lshl_add_u64 v[42:43], v[66:67], 0, v[42:43]
	v_min_u32_e32 v66, 0x400, v44
	v_add_u32_e32 v44, s58, v130
	v_ashrrev_i32_e32 v45, 31, v44
	v_lshl_add_u64 v[42:43], v[42:43], 4, s[20:21]
	v_lshl_add_u64 v[44:45], v[66:67], 0, v[44:45]
	v_lshl_add_u64 v[44:45], v[44:45], 4, s[20:21]
	global_load_dwordx4 v[54:57], v[42:43], off
	global_load_dwordx4 v[50:53], v[44:45], off
	v_add_u32_e32 v42, s95, v115
	v_max_i32_e32 v42, 3, v42
	v_add_u32_e32 v42, -3, v42
	v_add_u32_e32 v44, s95, v116
	v_min_u32_e32 v66, 0x400, v42
	v_add_u32_e32 v42, s58, v105
	v_max_i32_e32 v44, 3, v44
	v_ashrrev_i32_e32 v43, 31, v42
	v_add_u32_e32 v44, -3, v44
	v_lshl_add_u64 v[42:43], v[66:67], 0, v[42:43]
	v_min_u32_e32 v66, 0x400, v44
	v_add_u32_e32 v44, s58, v99
	v_ashrrev_i32_e32 v45, 31, v44
	v_lshl_add_u64 v[44:45], v[66:67], 0, v[44:45]
	v_lshl_add_u64 v[42:43], v[42:43], 4, s[20:21]
	v_lshl_add_u64 v[44:45], v[44:45], 4, s[20:21]
	global_load_dwordx4 v[46:49], v[42:43], off
	global_load_dwordx4 v[42:45], v[44:45], off
	s_branch .Lmy_k2_gdone
.Lmy_k2_gcopy:
	v_mov_b32_e32 v62, v220
	v_mov_b32_e32 v63, v221
	v_mov_b32_e32 v64, v222
	v_mov_b32_e32 v65, v223
	v_mov_b32_e32 v58, v224
	v_mov_b32_e32 v59, v225
	v_mov_b32_e32 v60, v226
	v_mov_b32_e32 v61, v227
	v_mov_b32_e32 v54, v228
	v_mov_b32_e32 v55, v229
	v_mov_b32_e32 v56, v230
	v_mov_b32_e32 v57, v231
	v_mov_b32_e32 v50, v232
	v_mov_b32_e32 v51, v233
	v_mov_b32_e32 v52, v234
	v_mov_b32_e32 v53, v235
	v_mov_b32_e32 v46, v236
	v_mov_b32_e32 v47, v237
	v_mov_b32_e32 v48, v238
	v_mov_b32_e32 v49, v239
	v_mov_b32_e32 v42, v240
	v_mov_b32_e32 v43, v241
	v_mov_b32_e32 v44, v242
	v_mov_b32_e32 v45, v243
.Lmy_k2_gdone:
	global_load_dwordx4 v[22:25], v106, s[56:57]
	global_load_dwordx4 v[26:29], v[2:3], off offset:1024
	global_load_dwordx4 v[30:33], v[4:5], off offset:2048
	v_add_co_u32_e32 v2, vcc, s43, v18
	s_nop 0
	v_addc_co_u32_e32 v3, vcc, 0, v19, vcc
	v_add_co_u32_e32 v4, vcc, s45, v18
	s_nop 0
	v_addc_co_u32_e32 v5, vcc, 0, v19, vcc
	global_load_dwordx4 v[34:37], v[2:3], off offset:3072
	global_load_dwordx4 v[38:41], v[4:5], off
	v_add_co_u32_e32 v2, vcc, s47, v18
	s_nop 0
	v_addc_co_u32_e32 v3, vcc, 0, v19, vcc
	v_add_co_u32_e32 v6, vcc, s33, v18
	s_nop 0
	v_addc_co_u32_e32 v7, vcc, 0, v19, vcc
	v_add_co_u32_e32 v10, vcc, s49, v18
	v_addc_co_u32_e32 v11, vcc, 0, v19, vcc
	v_add_co_u32_e32 v14, vcc, s60, v18
	v_addc_co_u32_e32 v15, vcc, 0, v19, vcc
	v_add_co_u32_e32 v18, vcc, s61, v18
	s_nop 0
	v_addc_co_u32_e32 v19, vcc, 0, v19, vcc
	global_load_dwordx4 v[2:5], v[2:3], off offset:1024
	s_nop 0
	global_load_dwordx4 v[6:9], v[6:7], off offset:2048
	s_nop 0
	global_load_dwordx4 v[10:13], v[10:11], off offset:3072
	s_nop 0
	global_load_dwordx4 v[14:17], v[14:15], off
	global_load_dwordx4 v[18:21], v[18:19], off offset:1024
	s_nop 0
	s_nop 0
	s_cmp_gt_i32 s3, 63
	s_cbranch_scc0 .LBB3_22
	s_and_saveexec_b64 s[58:59], s[8:9]

.LBB3_12:
	s_or_b64 exec, exec, s[20:21]
	v_mov_b32_e32 v107, v67
	s_waitcnt vmcnt(5)
	ds_write_b128 v123, v[22:25] offset:35776
	ds_write_b128 v124, v[26:29] offset:40896
	ds_write_b128 v125, v[30:33] offset:46016
	ds_write_b128 v126, v[34:37] offset:51136
	ds_write_b128 v127, v[38:41] offset:56256
	v_lshl_add_u64 v[22:23], s[56:57], 0, v[106:107]
	v_add_co_u32_e32 v24, vcc, 0xc000, v22
	s_waitcnt lgkmcnt(0)
	s_nop 0
	v_addc_co_u32_e32 v25, vcc, 0, v23, vcc
	v_add_co_u32_e32 v28, vcc, 0xd000, v22
	s_barrier
	v_add_u32_e32 v196, 0x6f80, v129
	v_add_u32_e32 v197, 0x6f80, v123
	v_add_u32_e32 v198, 0x6f80, v124
	v_add_u32_e32 v199, 0x6f80, v125
	v_add_u32_e32 v200, 0x6f80, v126
	v_add_u32_e32 v201, 0x6f80, v127
	s_nop 0
	v_addc_co_u32_e32 v29, vcc, 0, v23, vcc
	v_add_co_u32_e32 v32, vcc, 0xf000, v22
	s_nop 1
	v_addc_co_u32_e32 v33, vcc, 0, v23, vcc
	v_add_co_u32_e32 v36, vcc, 0x10000, v22
	global_load_dwordx4 v[24:27], v[24:25], off offset:2048
	s_nop 0
	global_load_dwordx4 v[28:31], v[28:29], off offset:3072
	v_addc_co_u32_e32 v37, vcc, 0, v23, vcc
	v_add_co_u32_e32 v40, vcc, 0x11000, v22
	global_load_dwordx4 v[32:35], v[32:33], off
	s_nop 0
	global_load_dwordx4 v[36:39], v[36:37], off offset:1024
	v_addc_co_u32_e32 v41, vcc, 0, v23, vcc
	global_load_dwordx4 v[40:43], v[40:41], off offset:2048
	s_waitcnt vmcnt(5)
	ds_write_b128 v197, v[2:5] offset:35776
	ds_write_b128 v198, v[6:9] offset:40896
	ds_write_b128 v199, v[10:13] offset:46016
	ds_write_b128 v200, v[14:17] offset:51136
	ds_write_b128 v201, v[18:21] offset:56256
	s_waitcnt vmcnt(5)
	ds_read_b128 v[44:47], v129 offset:35776
	ds_read_b128 v[48:51], v144
	ds_read_b128 v[52:55], v144 offset:64
	ds_read_b128 v[56:59], v129 offset:35840
	ds_read_b128 v[60:63], v129 offset:42432
	ds_read_b128 v[152:155], v129 offset:42496
	ds_read_b128 v[156:159], v129 offset:49088
	ds_read_b128 v[160:163], v129 offset:49152
	s_waitcnt lgkmcnt(6)
	v_mfma_f32_16x16x32_f16 v[44:47], v[44:47], v[48:51], 0
	ds_read_b128 v[164:167], v129 offset:55744
	ds_read_b128 v[168:171], v129 offset:55808
	s_waitcnt lgkmcnt(5)
	v_mfma_f32_16x16x32_f16 v[60:63], v[60:63], v[48:51], 0
	v_mfma_f32_16x16x32_f16 v[44:47], v[56:59], v[52:55], v[44:47]
	s_waitcnt lgkmcnt(4)
	v_mfma_f32_16x16x32_f16 v[56:59], v[152:155], v[52:55], v[60:63]
	ds_read_b128 v[152:155], v129 offset:35904
	s_waitcnt lgkmcnt(4)
	v_mfma_f32_16x16x32_f16 v[156:159], v[156:159], v[48:51], 0
	s_waitcnt lgkmcnt(2)
	v_mfma_f32_16x16x32_f16 v[48:51], v[164:167], v[48:51], 0
	v_mfma_f32_16x16x32_f16 v[60:63], v[160:163], v[52:55], v[156:159]
	s_waitcnt lgkmcnt(1)
	v_mfma_f32_16x16x32_f16 v[48:51], v[168:171], v[52:55], v[48:51]
	ds_read_b128 v[52:55], v144 offset:128
	s_nop 1
	ds_read_b128 v[156:159], v144 offset:192
	ds_read_b128 v[160:163], v129 offset:35968
	s_waitcnt lgkmcnt(2)
	v_mfma_f32_16x16x32_f16 v[44:47], v[152:155], v[52:55], v[44:47]
	ds_read_b128 v[152:155], v129 offset:42560
	ds_read_b128 v[164:167], v129 offset:42624
	s_waitcnt lgkmcnt(1)
	v_mfma_f32_16x16x32_f16 v[56:59], v[152:155], v[52:55], v[56:59]
	ds_read_b128 v[152:155], v129 offset:49216
	ds_read_b128 v[168:171], v129 offset:49280
	s_waitcnt lgkmcnt(1)
	v_mfma_f32_16x16x32_f16 v[60:63], v[152:155], v[52:55], v[60:63]
	ds_read_b128 v[152:155], v129 offset:55872
	ds_read_b128 v[172:175], v129 offset:55936
	s_waitcnt lgkmcnt(1)
	v_mfma_f32_16x16x32_f16 v[48:51], v[152:155], v[52:55], v[48:51]
	v_mfma_f32_16x16x32_f16 v[44:47], v[160:163], v[156:159], v[44:47]
	ds_read_b128 v[52:55], v144 offset:256
	ds_read_b128 v[152:155], v144 offset:320
	ds_read_b128 v[160:163], v129 offset:36032
	ds_read_b128 v[176:179], v129 offset:36096
	v_mfma_f32_16x16x32_f16 v[56:59], v[164:167], v[156:159], v[56:59]
	ds_read_b128 v[164:167], v129 offset:42688
	ds_read_b128 v[180:183], v129 offset:42752
	ds_read_b128 v[184:187], v129 offset:49344
	ds_read_b128 v[188:191], v129 offset:49408
	v_mfma_f32_16x16x32_f16 v[60:63], v[168:171], v[156:159], v[60:63]
	ds_read_b128 v[168:171], v129 offset:56000
	ds_read_b128 v[192:195], v129 offset:56064
	s_waitcnt lgkmcnt(0)
	v_mfma_f32_16x16x32_f16 v[48:51], v[172:175], v[156:159], v[48:51]
	v_add_co_u32_e32 v18, vcc, s75, v22
	v_mfma_f32_16x16x32_f16 v[2:5], v[160:163], v[52:55], v[44:47]
	s_nop 0
	v_addc_co_u32_e32 v19, vcc, 0, v23, vcc
	s_waitcnt lgkmcnt(0)
	v_add_co_u32_e32 v44, vcc, s76, v22
	v_mfma_f32_16x16x32_f16 v[14:17], v[168:171], v[52:55], v[48:51]
	s_nop 0
	v_addc_co_u32_e32 v45, vcc, 0, v23, vcc
	s_barrier
	v_add_co_u32_e32 v48, vcc, s77, v22
	v_mfma_f32_16x16x32_f16 v[6:9], v[164:167], v[52:55], v[56:59]
	s_nop 0
	v_addc_co_u32_e32 v49, vcc, 0, v23, vcc
	v_mfma_f32_16x16x32_f16 v[10:13], v[184:187], v[52:55], v[60:63]
	v_add_co_u32_e32 v52, vcc, s78, v22
	global_load_dwordx4 v[18:21], v[18:19], off offset:3072
	s_nop 0
	global_load_dwordx4 v[44:47], v[44:45], off
	v_addc_co_u32_e32 v53, vcc, 0, v23, vcc
	v_add_co_u32_e32 v56, vcc, s79, v22
	global_load_dwordx4 v[48:51], v[48:49], off offset:1024
	s_nop 0
	global_load_dwordx4 v[52:55], v[52:53], off offset:2048
	v_addc_co_u32_e32 v57, vcc, 0, v23, vcc
	global_load_dwordx4 v[56:59], v[56:57], off offset:3072
	s_waitcnt vmcnt(9)
	ds_write_b128 v123, v[24:27] offset:35776
	s_waitcnt vmcnt(8)
	ds_write_b128 v124, v[28:31] offset:40896
	s_waitcnt vmcnt(7)
	ds_write_b128 v125, v[32:35] offset:46016
	s_waitcnt vmcnt(6)
	ds_write_b128 v126, v[36:39] offset:51136
	s_waitcnt vmcnt(5)
	ds_write_b128 v127, v[40:43] offset:56256
	v_mfma_f32_16x16x32_f16 v[2:5], v[176:179], v[152:155], v[2:5]
	v_mfma_f32_16x16x32_f16 v[6:9], v[180:183], v[152:155], v[6:9]
	v_mfma_f32_16x16x32_f16 v[10:13], v[188:191], v[152:155], v[10:13]
	v_mfma_f32_16x16x32_f16 v[14:17], v[192:195], v[152:155], v[14:17]
	ds_read_b128 v[60:63], v196 offset:35776
	ds_read_b128 v[152:155], v144 offset:416
	ds_read_b128 v[208:211], v196 offset:42432
	ds_read_b128 v[212:215], v196 offset:49088
	ds_read_b128 v[216:219], v196 offset:55744
	ds_read_b128 v[156:159], v144 offset:480
	ds_read_b128 v[160:163], v196 offset:35840
	ds_read_b128 v[164:167], v196 offset:42496
	ds_read_b128 v[168:171], v196 offset:49152
	ds_read_b128 v[172:175], v196 offset:55808
	s_waitcnt lgkmcnt(8)
	v_mfma_f32_16x16x32_f16 v[2:5], v[60:63], v[152:155], v[2:5]
	s_waitcnt lgkmcnt(7)
	v_mfma_f32_16x16x32_f16 v[6:9], v[208:211], v[152:155], v[6:9]
	s_waitcnt lgkmcnt(6)
	v_mfma_f32_16x16x32_f16 v[10:13], v[212:215], v[152:155], v[10:13]
	s_waitcnt lgkmcnt(5)
	v_mfma_f32_16x16x32_f16 v[14:17], v[216:219], v[152:155], v[14:17]
	s_waitcnt lgkmcnt(0)
	ds_read_b128 v[60:63], v196 offset:35904
	v_mfma_f32_16x16x32_f16 v[2:5], v[160:163], v[156:159], v[2:5]
	v_mfma_f32_16x16x32_f16 v[6:9], v[164:167], v[156:159], v[6:9]
	v_mfma_f32_16x16x32_f16 v[10:13], v[168:171], v[156:159], v[10:13]
	s_waitcnt lgkmcnt(1)
	v_mfma_f32_16x16x32_f16 v[14:17], v[172:175], v[156:159], v[14:17]
	ds_read_b128 v[152:155], v144 offset:544
	ds_read_b128 v[208:211], v196 offset:42560
	ds_read_b128 v[212:215], v196 offset:49216
	ds_read_b128 v[216:219], v196 offset:55872
	ds_read_b128 v[156:159], v144 offset:608
	ds_read_b128 v[160:163], v196 offset:35968
	ds_read_b128 v[164:167], v196 offset:42624
	ds_read_b128 v[168:171], v196 offset:49280
	ds_read_b128 v[172:175], v196 offset:55936
	s_waitcnt lgkmcnt(8)
	v_mfma_f32_16x16x32_f16 v[2:5], v[60:63], v[152:155], v[2:5]
	s_waitcnt lgkmcnt(7)
	v_mfma_f32_16x16x32_f16 v[6:9], v[208:211], v[152:155], v[6:9]
	s_waitcnt lgkmcnt(6)
	v_mfma_f32_16x16x32_f16 v[10:13], v[212:215], v[152:155], v[10:13]
	s_waitcnt lgkmcnt(5)
	v_mfma_f32_16x16x32_f16 v[14:17], v[216:219], v[152:155], v[14:17]
	s_waitcnt lgkmcnt(0)
	v_mfma_f32_16x16x32_f16 v[2:5], v[160:163], v[156:159], v[2:5]
	ds_read_b128 v[60:63], v144 offset:672
	ds_read_b128 v[152:155], v144 offset:736
	ds_read_b128 v[160:163], v196 offset:36032
	ds_read_b128 v[176:179], v196 offset:36096
	v_mfma_f32_16x16x32_f16 v[6:9], v[164:167], v[156:159], v[6:9]
	ds_read_b128 v[164:167], v196 offset:42688
	ds_read_b128 v[180:183], v196 offset:42752
	ds_read_b128 v[184:187], v196 offset:49344
	ds_read_b128 v[188:191], v196 offset:49408
	v_mfma_f32_16x16x32_f16 v[10:13], v[168:171], v[156:159], v[10:13]
	ds_read_b128 v[168:171], v196 offset:56000
	ds_read_b128 v[192:195], v196 offset:56064
	s_waitcnt lgkmcnt(0)
	v_add_co_u32_e32 v24, vcc, s80, v22
	v_addc_co_u32_e32 v25, vcc, 0, v23, vcc
	v_add_co_u32_e32 v28, vcc, s81, v22
	s_waitcnt lgkmcnt(0)
	s_nop 0
	v_addc_co_u32_e32 v29, vcc, 0, v23, vcc
	v_add_co_u32_e32 v32, vcc, s82, v22
	s_barrier
	s_nop 0
	v_addc_co_u32_e32 v33, vcc, 0, v23, vcc
	v_add_co_u32_e32 v36, vcc, s83, v22
	s_nop 1
	v_addc_co_u32_e32 v37, vcc, 0, v23, vcc
	v_add_co_u32_e32 v40, vcc, s84, v22
	global_load_dwordx4 v[24:27], v[24:25], off
	s_nop 0
	global_load_dwordx4 v[28:31], v[28:29], off offset:1024
	s_nop 0
	global_load_dwordx4 v[32:35], v[32:33], off offset:2048
	s_nop 0
	global_load_dwordx4 v[36:39], v[36:37], off offset:3072
	v_addc_co_u32_e32 v41, vcc, 0, v23, vcc
	global_load_dwordx4 v[40:43], v[40:41], off
	s_waitcnt vmcnt(9)
	ds_write_b128 v197, v[18:21] offset:35776
	s_waitcnt vmcnt(8)
	ds_write_b128 v198, v[44:47] offset:40896
	s_waitcnt vmcnt(7)
	ds_write_b128 v199, v[48:51] offset:46016
	s_waitcnt vmcnt(6)
	ds_write_b128 v200, v[52:55] offset:51136
	s_waitcnt vmcnt(5)
	ds_write_b128 v201, v[56:59] offset:56256
	v_mfma_f32_16x16x32_f16 v[14:17], v[172:175], v[156:159], v[14:17]
	v_mfma_f32_16x16x32_f16 v[2:5], v[160:163], v[60:63], v[2:5]
	v_mfma_f32_16x16x32_f16 v[6:9], v[164:167], v[60:63], v[6:9]
	v_mfma_f32_16x16x32_f16 v[10:13], v[184:187], v[60:63], v[10:13]
	v_mfma_f32_16x16x32_f16 v[14:17], v[168:171], v[60:63], v[14:17]
	v_mfma_f32_16x16x32_f16 v[2:5], v[176:179], v[152:155], v[2:5]
	v_mfma_f32_16x16x32_f16 v[6:9], v[180:183], v[152:155], v[6:9]
	v_mfma_f32_16x16x32_f16 v[10:13], v[188:191], v[152:155], v[10:13]
	v_mfma_f32_16x16x32_f16 v[14:17], v[192:195], v[152:155], v[14:17]
	ds_read_b128 v[60:63], v129 offset:35776
	ds_read_b128 v[152:155], v144 offset:832
	ds_read_b128 v[208:211], v129 offset:42432
	ds_read_b128 v[212:215], v129 offset:49088
	ds_read_b128 v[216:219], v129 offset:55744
	ds_read_b128 v[156:159], v144 offset:896
	ds_read_b128 v[160:163], v129 offset:35840
	ds_read_b128 v[164:167], v129 offset:42496
	ds_read_b128 v[168:171], v129 offset:49152
	ds_read_b128 v[172:175], v129 offset:55808
	s_waitcnt lgkmcnt(8)
	v_mfma_f32_16x16x32_f16 v[2:5], v[60:63], v[152:155], v[2:5]
	s_waitcnt lgkmcnt(7)
	v_mfma_f32_16x16x32_f16 v[6:9], v[208:211], v[152:155], v[6:9]
	s_waitcnt lgkmcnt(6)
	v_mfma_f32_16x16x32_f16 v[10:13], v[212:215], v[152:155], v[10:13]
	s_waitcnt lgkmcnt(5)
	v_mfma_f32_16x16x32_f16 v[14:17], v[216:219], v[152:155], v[14:17]
	s_waitcnt lgkmcnt(0)
	ds_read_b128 v[60:63], v129 offset:35904
	v_mfma_f32_16x16x32_f16 v[2:5], v[160:163], v[156:159], v[2:5]
	v_mfma_f32_16x16x32_f16 v[6:9], v[164:167], v[156:159], v[6:9]
	v_mfma_f32_16x16x32_f16 v[10:13], v[168:171], v[156:159], v[10:13]
	s_waitcnt lgkmcnt(1)
	v_mfma_f32_16x16x32_f16 v[14:17], v[172:175], v[156:159], v[14:17]
	ds_read_b128 v[152:155], v144 offset:960
	ds_read_b128 v[208:211], v129 offset:42560
	ds_read_b128 v[212:215], v129 offset:49216
	ds_read_b128 v[216:219], v129 offset:55872
	ds_read_b128 v[156:159], v144 offset:1024
	ds_read_b128 v[160:163], v129 offset:35968
	ds_read_b128 v[164:167], v129 offset:42624
	ds_read_b128 v[168:171], v129 offset:49280
	ds_read_b128 v[172:175], v129 offset:55936
	s_waitcnt lgkmcnt(8)
	v_mfma_f32_16x16x32_f16 v[2:5], v[60:63], v[152:155], v[2:5]
	s_waitcnt lgkmcnt(7)
	v_mfma_f32_16x16x32_f16 v[6:9], v[208:211], v[152:155], v[6:9]
	s_waitcnt lgkmcnt(6)
	v_mfma_f32_16x16x32_f16 v[10:13], v[212:215], v[152:155], v[10:13]
	s_waitcnt lgkmcnt(5)
	v_mfma_f32_16x16x32_f16 v[14:17], v[216:219], v[152:155], v[14:17]
	s_waitcnt lgkmcnt(0)
	v_mfma_f32_16x16x32_f16 v[2:5], v[160:163], v[156:159], v[2:5]
	ds_read_b128 v[60:63], v144 offset:1088
	ds_read_b128 v[152:155], v144 offset:1152
	ds_read_b128 v[160:163], v129 offset:36032
	ds_read_b128 v[176:179], v129 offset:36096
	v_mfma_f32_16x16x32_f16 v[6:9], v[164:167], v[156:159], v[6:9]
	ds_read_b128 v[164:167], v129 offset:42688
	ds_read_b128 v[180:183], v129 offset:42752
	ds_read_b128 v[184:187], v129 offset:49344
	ds_read_b128 v[188:191], v129 offset:49408
	v_mfma_f32_16x16x32_f16 v[10:13], v[168:171], v[156:159], v[10:13]
	ds_read_b128 v[168:171], v129 offset:56000
	ds_read_b128 v[192:195], v129 offset:56064
	s_waitcnt lgkmcnt(0)
	v_add_co_u32_e32 v18, vcc, s85, v22
	v_addc_co_u32_e32 v19, vcc, 0, v23, vcc
	v_add_co_u32_e32 v44, vcc, s27, v22
	s_waitcnt lgkmcnt(0)
	s_nop 0
	v_addc_co_u32_e32 v45, vcc, 0, v23, vcc
	v_add_co_u32_e32 v48, vcc, s86, v22
	s_barrier
	s_nop 0
	v_addc_co_u32_e32 v49, vcc, 0, v23, vcc
	v_add_co_u32_e32 v52, vcc, s87, v22
	s_nop 1
	v_addc_co_u32_e32 v53, vcc, 0, v23, vcc
	v_add_co_u32_e32 v56, vcc, s88, v22
	global_load_dwordx4 v[18:21], v[18:19], off offset:1024
	s_nop 0
	global_load_dwordx4 v[44:47], v[44:45], off offset:2048
	s_nop 0
	global_load_dwordx4 v[48:51], v[48:49], off offset:3072
	s_nop 0
	global_load_dwordx4 v[52:55], v[52:53], off
	v_addc_co_u32_e32 v57, vcc, 0, v23, vcc
	global_load_dwordx4 v[56:59], v[56:57], off offset:1024
	s_waitcnt vmcnt(9)
	ds_write_b128 v123, v[24:27] offset:35776
	s_waitcnt vmcnt(8)
	ds_write_b128 v124, v[28:31] offset:40896
	s_waitcnt vmcnt(7)
	ds_write_b128 v125, v[32:35] offset:46016
	s_waitcnt vmcnt(6)
	ds_write_b128 v126, v[36:39] offset:51136
	s_waitcnt vmcnt(5)
	ds_write_b128 v127, v[40:43] offset:56256
	v_mfma_f32_16x16x32_f16 v[14:17], v[172:175], v[156:159], v[14:17]
	v_mfma_f32_16x16x32_f16 v[2:5], v[160:163], v[60:63], v[2:5]
	v_mfma_f32_16x16x32_f16 v[6:9], v[164:167], v[60:63], v[6:9]
	v_mfma_f32_16x16x32_f16 v[10:13], v[184:187], v[60:63], v[10:13]
	v_mfma_f32_16x16x32_f16 v[14:17], v[168:171], v[60:63], v[14:17]
	v_mfma_f32_16x16x32_f16 v[2:5], v[176:179], v[152:155], v[2:5]
	v_mfma_f32_16x16x32_f16 v[6:9], v[180:183], v[152:155], v[6:9]
	v_mfma_f32_16x16x32_f16 v[10:13], v[188:191], v[152:155], v[10:13]
	v_mfma_f32_16x16x32_f16 v[14:17], v[192:195], v[152:155], v[14:17]
	ds_read_b128 v[60:63], v196 offset:35776
	ds_read_b128 v[152:155], v144 offset:1248
	ds_read_b128 v[208:211], v196 offset:42432
	ds_read_b128 v[212:215], v196 offset:49088
	ds_read_b128 v[216:219], v196 offset:55744
	ds_read_b128 v[156:159], v144 offset:1312
	ds_read_b128 v[160:163], v196 offset:35840
	ds_read_b128 v[164:167], v196 offset:42496
	ds_read_b128 v[168:171], v196 offset:49152
	ds_read_b128 v[172:175], v196 offset:55808
	s_waitcnt lgkmcnt(8)
	v_mfma_f32_16x16x32_f16 v[2:5], v[60:63], v[152:155], v[2:5]
	s_waitcnt lgkmcnt(7)
	v_mfma_f32_16x16x32_f16 v[6:9], v[208:211], v[152:155], v[6:9]
	s_waitcnt lgkmcnt(6)
	v_mfma_f32_16x16x32_f16 v[10:13], v[212:215], v[152:155], v[10:13]
	s_waitcnt lgkmcnt(5)
	v_mfma_f32_16x16x32_f16 v[14:17], v[216:219], v[152:155], v[14:17]
	s_waitcnt lgkmcnt(0)
	ds_read_b128 v[60:63], v196 offset:35904
	v_mfma_f32_16x16x32_f16 v[2:5], v[160:163], v[156:159], v[2:5]
	v_mfma_f32_16x16x32_f16 v[6:9], v[164:167], v[156:159], v[6:9]
	v_mfma_f32_16x16x32_f16 v[10:13], v[168:171], v[156:159], v[10:13]
	s_waitcnt lgkmcnt(1)
	v_mfma_f32_16x16x32_f16 v[14:17], v[172:175], v[156:159], v[14:17]
	ds_read_b128 v[152:155], v144 offset:1376
	ds_read_b128 v[208:211], v196 offset:42560
	ds_read_b128 v[212:215], v196 offset:49216
	ds_read_b128 v[216:219], v196 offset:55872
	ds_read_b128 v[156:159], v144 offset:1440
	ds_read_b128 v[160:163], v196 offset:35968
	ds_read_b128 v[164:167], v196 offset:42624
	ds_read_b128 v[168:171], v196 offset:49280
	ds_read_b128 v[172:175], v196 offset:55936
	s_waitcnt lgkmcnt(8)
	v_mfma_f32_16x16x32_f16 v[2:5], v[60:63], v[152:155], v[2:5]
	s_waitcnt lgkmcnt(7)
	v_mfma_f32_16x16x32_f16 v[6:9], v[208:211], v[152:155], v[6:9]
	s_waitcnt lgkmcnt(6)
	v_mfma_f32_16x16x32_f16 v[10:13], v[212:215], v[152:155], v[10:13]
	s_waitcnt lgkmcnt(5)
	v_mfma_f32_16x16x32_f16 v[14:17], v[216:219], v[152:155], v[14:17]
	s_waitcnt lgkmcnt(0)
	v_mfma_f32_16x16x32_f16 v[2:5], v[160:163], v[156:159], v[2:5]
	ds_read_b128 v[60:63], v144 offset:1504
	ds_read_b128 v[152:155], v144 offset:1568
	ds_read_b128 v[160:163], v196 offset:36032
	ds_read_b128 v[176:179], v196 offset:36096
	v_mfma_f32_16x16x32_f16 v[6:9], v[164:167], v[156:159], v[6:9]
	ds_read_b128 v[164:167], v196 offset:42688
	ds_read_b128 v[180:183], v196 offset:42752
	ds_read_b128 v[184:187], v196 offset:49344
	ds_read_b128 v[188:191], v196 offset:49408
	v_mfma_f32_16x16x32_f16 v[10:13], v[168:171], v[156:159], v[10:13]
	ds_read_b128 v[168:171], v196 offset:56000
	ds_read_b128 v[192:195], v196 offset:56064
	s_waitcnt lgkmcnt(0)
	v_add_co_u32_e32 v24, vcc, s89, v22
	v_addc_co_u32_e32 v25, vcc, 0, v23, vcc
	v_add_co_u32_e32 v28, vcc, s90, v22
	s_waitcnt lgkmcnt(0)
	s_nop 0
	v_addc_co_u32_e32 v29, vcc, 0, v23, vcc
	v_add_co_u32_e32 v32, vcc, s91, v22
	s_barrier
	s_nop 0
	v_addc_co_u32_e32 v33, vcc, 0, v23, vcc
	v_add_co_u32_e32 v36, vcc, s92, v22
	s_nop 1
	v_addc_co_u32_e32 v37, vcc, 0, v23, vcc
	v_add_co_u32_e32 v22, vcc, s93, v22
	global_load_dwordx4 v[24:27], v[24:25], off offset:2048
	s_nop 0
	global_load_dwordx4 v[28:31], v[28:29], off offset:3072
	s_nop 0
	global_load_dwordx4 v[32:35], v[32:33], off
	s_nop 0
	global_load_dwordx4 v[36:39], v[36:37], off offset:1024
	v_addc_co_u32_e32 v23, vcc, 0, v23, vcc
	global_load_dwordx4 v[40:43], v[22:23], off offset:2048
	s_waitcnt vmcnt(9)
	ds_write_b128 v197, v[18:21] offset:35776
	s_waitcnt vmcnt(8)
	ds_write_b128 v198, v[44:47] offset:40896
	s_waitcnt vmcnt(7)
	ds_write_b128 v199, v[48:51] offset:46016
	s_waitcnt vmcnt(6)
	ds_write_b128 v200, v[52:55] offset:51136
	s_waitcnt vmcnt(5)
	ds_write_b128 v201, v[56:59] offset:56256
	s_mul_i32 s98, s94, 0x50
	s_addk_i32 s98, 0x50
	s_mul_i32 s99, s94, 0xffe9a800
	s_add_i32 s99, s99, s29
	v_mov_b32_e32 v249, 0
	v_add_u32_e32 v244, s98, v1
	v_max_i32_e32 v244, 3, v244
	v_add_u32_e32 v244, -3, v244
	v_add_u32_e32 v246, s98, v112
	v_min_u32_e32 v248, 0x400, v244
	v_add_u32_e32 v244, s99, v133
	v_max_i32_e32 v246, 3, v246
	v_ashrrev_i32_e32 v245, 31, v244
	v_add_u32_e32 v246, -3, v246
	v_lshl_add_u64 v[244:245], v[248:249], 0, v[244:245]
	v_min_u32_e32 v248, 0x400, v246
	v_add_u32_e32 v246, s99, v132
	v_ashrrev_i32_e32 v247, 31, v246
	v_lshl_add_u64 v[244:245], v[244:245], 4, s[36:37]
	v_lshl_add_u64 v[246:247], v[248:249], 0, v[246:247]
	v_lshl_add_u64 v[246:247], v[246:247], 4, s[36:37]
	global_load_dwordx4 v[220:223], v[244:245], off
	global_load_dwordx4 v[224:227], v[246:247], off
	v_add_u32_e32 v244, s98, v113
	v_max_i32_e32 v244, 3, v244
	v_add_u32_e32 v244, -3, v244
	v_add_u32_e32 v246, s98, v114
	v_min_u32_e32 v248, 0x400, v244
	v_add_u32_e32 v244, s99, v131
	v_max_i32_e32 v246, 3, v246
	v_ashrrev_i32_e32 v245, 31, v244
	v_add_u32_e32 v246, -3, v246
	v_lshl_add_u64 v[244:245], v[248:249], 0, v[244:245]
	v_min_u32_e32 v248, 0x400, v246
	v_add_u32_e32 v246, s99, v130
	v_ashrrev_i32_e32 v247, 31, v246
	v_lshl_add_u64 v[244:245], v[244:245], 4, s[36:37]
	v_lshl_add_u64 v[246:247], v[248:249], 0, v[246:247]
	v_lshl_add_u64 v[246:247], v[246:247], 4, s[36:37]
	global_load_dwordx4 v[228:231], v[244:245], off
	global_load_dwordx4 v[232:235], v[246:247], off
	v_add_u32_e32 v244, s98, v115
	v_max_i32_e32 v244, 3, v244
	v_add_u32_e32 v244, -3, v244
	v_add_u32_e32 v246, s98, v116
	v_min_u32_e32 v248, 0x400, v244
	v_add_u32_e32 v244, s99, v105
	v_max_i32_e32 v246, 3, v246
	v_ashrrev_i32_e32 v245, 31, v244
	v_add_u32_e32 v246, -3, v246
	v_lshl_add_u64 v[244:245], v[248:249], 0, v[244:245]
	v_min_u32_e32 v248, 0x400, v246
	v_add_u32_e32 v246, s99, v99
	v_ashrrev_i32_e32 v247, 31, v246
	v_lshl_add_u64 v[246:247], v[248:249], 0, v[246:247]
	v_lshl_add_u64 v[244:245], v[244:245], 4, s[36:37]
	v_lshl_add_u64 v[246:247], v[246:247], 4, s[36:37]
	global_load_dwordx4 v[236:239], v[244:245], off
	global_load_dwordx4 v[240:243], v[246:247], off
	v_mfma_f32_16x16x32_f16 v[14:17], v[172:175], v[156:159], v[14:17]
	v_mfma_f32_16x16x32_f16 v[2:5], v[160:163], v[60:63], v[2:5]
	v_mfma_f32_16x16x32_f16 v[6:9], v[164:167], v[60:63], v[6:9]
	v_mfma_f32_16x16x32_f16 v[10:13], v[184:187], v[60:63], v[10:13]
	v_mfma_f32_16x16x32_f16 v[14:17], v[168:171], v[60:63], v[14:17]
	v_mfma_f32_16x16x32_f16 v[2:5], v[176:179], v[152:155], v[2:5]
	v_mfma_f32_16x16x32_f16 v[6:9], v[180:183], v[152:155], v[6:9]
	v_mfma_f32_16x16x32_f16 v[10:13], v[188:191], v[152:155], v[10:13]
	v_mfma_f32_16x16x32_f16 v[14:17], v[192:195], v[152:155], v[14:17]
	ds_read_b128 v[60:63], v129 offset:35776
	ds_read_b128 v[152:155], v144 offset:1664
	ds_read_b128 v[208:211], v129 offset:42432
	ds_read_b128 v[212:215], v129 offset:49088
	ds_read_b128 v[216:219], v129 offset:55744
	ds_read_b128 v[156:159], v144 offset:1728
	ds_read_b128 v[160:163], v129 offset:35840
	ds_read_b128 v[164:167], v129 offset:42496
	ds_read_b128 v[168:171], v129 offset:49152
	ds_read_b128 v[172:175], v129 offset:55808
	s_waitcnt lgkmcnt(8)
	v_mfma_f32_16x16x32_f16 v[2:5], v[60:63], v[152:155], v[2:5]
	s_waitcnt lgkmcnt(7)
	v_mfma_f32_16x16x32_f16 v[6:9], v[208:211], v[152:155], v[6:9]
	s_waitcnt lgkmcnt(6)
	v_mfma_f32_16x16x32_f16 v[10:13], v[212:215], v[152:155], v[10:13]
	s_waitcnt lgkmcnt(5)
	v_mfma_f32_16x16x32_f16 v[14:17], v[216:219], v[152:155], v[14:17]
	s_waitcnt lgkmcnt(0)
	ds_read_b128 v[60:63], v129 offset:35904
	v_mfma_f32_16x16x32_f16 v[2:5], v[160:163], v[156:159], v[2:5]
	v_mfma_f32_16x16x32_f16 v[6:9], v[164:167], v[156:159], v[6:9]
	v_mfma_f32_16x16x32_f16 v[10:13], v[168:171], v[156:159], v[10:13]
	s_waitcnt lgkmcnt(1)
	v_mfma_f32_16x16x32_f16 v[14:17], v[172:175], v[156:159], v[14:17]
	ds_read_b128 v[152:155], v144 offset:1792
	ds_read_b128 v[208:211], v129 offset:42560
	ds_read_b128 v[212:215], v129 offset:49216
	ds_read_b128 v[216:219], v129 offset:55872
	ds_read_b128 v[156:159], v144 offset:1856
	ds_read_b128 v[160:163], v129 offset:35968
	ds_read_b128 v[164:167], v129 offset:42624
	ds_read_b128 v[168:171], v129 offset:49280
	ds_read_b128 v[172:175], v129 offset:55936
	s_waitcnt lgkmcnt(8)
	v_mfma_f32_16x16x32_f16 v[2:5], v[60:63], v[152:155], v[2:5]
	s_waitcnt lgkmcnt(7)
	v_mfma_f32_16x16x32_f16 v[6:9], v[208:211], v[152:155], v[6:9]
	s_waitcnt lgkmcnt(6)
	v_mfma_f32_16x16x32_f16 v[10:13], v[212:215], v[152:155], v[10:13]
	s_waitcnt lgkmcnt(5)
	v_mfma_f32_16x16x32_f16 v[14:17], v[216:219], v[152:155], v[14:17]
	s_waitcnt lgkmcnt(0)
	ds_read_b128 v[60:63], v129 offset:36032
	v_mfma_f32_16x16x32_f16 v[2:5], v[160:163], v[156:159], v[2:5]
	v_mfma_f32_16x16x32_f16 v[6:9], v[164:167], v[156:159], v[6:9]
	v_mfma_f32_16x16x32_f16 v[10:13], v[168:171], v[156:159], v[10:13]
	s_waitcnt lgkmcnt(1)
	v_mfma_f32_16x16x32_f16 v[14:17], v[172:175], v[156:159], v[14:17]
	ds_read_b128 v[152:155], v144 offset:1920
	ds_read_b128 v[156:159], v144 offset:1984
	ds_read_b128 v[160:163], v129 offset:36096
	s_waitcnt lgkmcnt(2)
	v_mfma_f32_16x16x32_f16 v[2:5], v[60:63], v[152:155], v[2:5]
	ds_read_b128 v[60:63], v129 offset:42688
	ds_read_b128 v[164:167], v129 offset:42752
	s_waitcnt lgkmcnt(1)
	v_mfma_f32_16x16x32_f16 v[6:9], v[60:63], v[152:155], v[6:9]
	ds_read_b128 v[60:63], v129 offset:49344
	ds_read_b128 v[168:171], v129 offset:49408
	s_waitcnt lgkmcnt(1)
	v_mfma_f32_16x16x32_f16 v[10:13], v[60:63], v[152:155], v[10:13]
	ds_read_b128 v[60:63], v129 offset:56000
	ds_read_b128 v[172:175], v129 offset:56064
	s_waitcnt lgkmcnt(0)
	v_mfma_f32_16x16x32_f16 v[14:17], v[60:63], v[152:155], v[14:17]
	v_mfma_f32_16x16x32_f16 v[2:5], v[160:163], v[156:159], v[2:5]
	s_waitcnt lgkmcnt(0)
	s_barrier
	s_waitcnt vmcnt(10)
	ds_write_b128 v123, v[24:27] offset:35776
	s_waitcnt vmcnt(9)
	ds_write_b128 v124, v[28:31] offset:40896
	s_waitcnt vmcnt(8)
	ds_write_b128 v125, v[32:35] offset:46016
	s_waitcnt vmcnt(7)
	ds_write_b128 v126, v[36:39] offset:51136
	s_waitcnt vmcnt(6)
	ds_write_b128 v127, v[40:43] offset:56256
	v_mfma_f32_16x16x32_f16 v[6:9], v[164:167], v[156:159], v[6:9]
	v_mfma_f32_16x16x32_f16 v[10:13], v[168:171], v[156:159], v[10:13]
	v_mfma_f32_16x16x32_f16 v[14:17], v[172:175], v[156:159], v[14:17]
	ds_read_b128 v[18:21], v196 offset:35776
	ds_read_b128 v[44:47], v144 offset:2080
	ds_read_b128 v[48:51], v144 offset:2144
	ds_read_b128 v[52:55], v196 offset:35840
	s_waitcnt lgkmcnt(2)
	v_mfma_f32_16x16x32_f16 v[2:5], v[18:21], v[44:47], v[2:5]
	ds_read_b128 v[18:21], v196 offset:42432
	ds_read_b128 v[56:59], v196 offset:42496
	s_waitcnt lgkmcnt(1)
	v_mfma_f32_16x16x32_f16 v[6:9], v[18:21], v[44:47], v[6:9]
	ds_read_b128 v[18:21], v196 offset:49088
	ds_read_b128 v[60:63], v196 offset:49152
	s_waitcnt lgkmcnt(1)
	v_mfma_f32_16x16x32_f16 v[10:13], v[18:21], v[44:47], v[10:13]
	ds_read_b128 v[18:21], v196 offset:55744
	ds_read_b128 v[152:155], v196 offset:55808
	s_waitcnt lgkmcnt(1)
	v_mfma_f32_16x16x32_f16 v[14:17], v[18:21], v[44:47], v[14:17]
	ds_read_b128 v[18:21], v196 offset:35904
	v_mfma_f32_16x16x32_f16 v[2:5], v[52:55], v[48:51], v[2:5]
	v_mfma_f32_16x16x32_f16 v[6:9], v[56:59], v[48:51], v[6:9]
	v_mfma_f32_16x16x32_f16 v[10:13], v[60:63], v[48:51], v[10:13]
	s_waitcnt lgkmcnt(1)
	v_mfma_f32_16x16x32_f16 v[14:17], v[152:155], v[48:51], v[14:17]
	ds_read_b128 v[44:47], v144 offset:2208
	ds_read_b128 v[48:51], v144 offset:2272
	ds_read_b128 v[52:55], v196 offset:35968
	s_waitcnt lgkmcnt(2)
	v_mfma_f32_16x16x32_f16 v[2:5], v[18:21], v[44:47], v[2:5]
	ds_read_b128 v[18:21], v196 offset:42560
	ds_read_b128 v[56:59], v196 offset:42624
	s_waitcnt lgkmcnt(1)
	v_mfma_f32_16x16x32_f16 v[6:9], v[18:21], v[44:47], v[6:9]
	ds_read_b128 v[18:21], v196 offset:49216
	ds_read_b128 v[60:63], v196 offset:49280
	s_waitcnt lgkmcnt(1)
	v_mfma_f32_16x16x32_f16 v[10:13], v[18:21], v[44:47], v[10:13]
	ds_read_b128 v[18:21], v196 offset:55872
	ds_read_b128 v[152:155], v196 offset:55936
	s_waitcnt lgkmcnt(1)
	v_mfma_f32_16x16x32_f16 v[14:17], v[18:21], v[44:47], v[14:17]
	ds_read_b128 v[18:21], v196 offset:36032
	v_mfma_f32_16x16x32_f16 v[2:5], v[52:55], v[48:51], v[2:5]
	v_mfma_f32_16x16x32_f16 v[6:9], v[56:59], v[48:51], v[6:9]
	v_mfma_f32_16x16x32_f16 v[10:13], v[60:63], v[48:51], v[10:13]
	s_waitcnt lgkmcnt(1)
	v_mfma_f32_16x16x32_f16 v[14:17], v[152:155], v[48:51], v[14:17]
	ds_read_b128 v[44:47], v144 offset:2336
	ds_read_b128 v[48:51], v144 offset:2400
	ds_read_b128 v[52:55], v196 offset:36096
	s_waitcnt lgkmcnt(2)
	v_mfma_f32_16x16x32_f16 v[2:5], v[18:21], v[44:47], v[2:5]
	ds_read_b128 v[18:21], v196 offset:42688
	ds_read_b128 v[56:59], v196 offset:42752
	s_waitcnt lgkmcnt(1)
	v_mfma_f32_16x16x32_f16 v[6:9], v[18:21], v[44:47], v[6:9]
	ds_read_b128 v[18:21], v196 offset:49344
	ds_read_b128 v[60:63], v196 offset:49408
	s_waitcnt lgkmcnt(1)
	v_mfma_f32_16x16x32_f16 v[10:13], v[18:21], v[44:47], v[10:13]
	ds_read_b128 v[18:21], v196 offset:56000
	ds_read_b128 v[152:155], v196 offset:56064
	s_waitcnt lgkmcnt(0)
	v_mfma_f32_16x16x32_f16 v[14:17], v[18:21], v[44:47], v[14:17]
	v_mfma_f32_16x16x32_f16 v[2:5], v[52:55], v[48:51], v[2:5]
	s_waitcnt lgkmcnt(0)
	s_barrier
	v_mfma_f32_16x16x32_f16 v[6:9], v[56:59], v[48:51], v[6:9]
	v_mfma_f32_16x16x32_f16 v[10:13], v[60:63], v[48:51], v[10:13]
	v_mfma_f32_16x16x32_f16 v[14:17], v[152:155], v[48:51], v[14:17]
	ds_read_b128 v[18:21], v129 offset:35776
	ds_read_b128 v[22:25], v144 offset:2496
	ds_read_b128 v[26:29], v144 offset:2560
	ds_read_b128 v[30:33], v129 offset:35840
	s_waitcnt lgkmcnt(2)
	v_mfma_f32_16x16x32_f16 v[2:5], v[18:21], v[22:25], v[2:5]
	ds_read_b128 v[18:21], v129 offset:42432
	ds_read_b128 v[34:37], v129 offset:42496
	s_waitcnt lgkmcnt(1)
	v_mfma_f32_16x16x32_f16 v[6:9], v[18:21], v[22:25], v[6:9]
	ds_read_b128 v[18:21], v129 offset:49088
	ds_read_b128 v[38:41], v129 offset:49152
	s_waitcnt lgkmcnt(1)
	v_mfma_f32_16x16x32_f16 v[10:13], v[18:21], v[22:25], v[10:13]
	ds_read_b128 v[18:21], v129 offset:55744
	ds_read_b128 v[42:45], v129 offset:55808
	s_waitcnt lgkmcnt(1)
	v_mfma_f32_16x16x32_f16 v[14:17], v[18:21], v[22:25], v[14:17]
	v_mfma_f32_16x16x32_f16 v[2:5], v[30:33], v[26:29], v[2:5]
	ds_read_b128 v[18:21], v144 offset:2624
	ds_read_b128 v[22:25], v144 offset:2688
	ds_read_b128 v[30:33], v129 offset:35904
	ds_read_b128 v[46:49], v129 offset:35968
	s_waitcnt lgkmcnt(1)
	v_mfma_f32_16x16x32_f16 v[2:5], v[30:33], v[18:21], v[2:5]
	v_mfma_f32_16x16x32_f16 v[6:9], v[34:37], v[26:29], v[6:9]
	ds_read_b128 v[34:37], v129 offset:42560
	ds_read_b128 v[50:53], v129 offset:42624
	ds_read_b128 v[54:57], v129 offset:49216
	ds_read_b128 v[58:61], v129 offset:49280
	v_mfma_f32_16x16x32_f16 v[10:13], v[38:41], v[26:29], v[10:13]
	ds_read_b128 v[38:41], v129 offset:55872
	ds_read_b128 v[62:65], v129 offset:55936
	ds_read_b128 v[152:155], v129 offset:36032
	ds_read_b128 v[30:33], v144 offset:2752
	ds_read_b128 v[156:159], v144 offset:2816
	ds_read_b128 v[160:163], v129 offset:36096
	s_waitcnt lgkmcnt(10)
	v_mfma_f32_16x16x32_f16 v[2:5], v[46:49], v[22:25], v[2:5]
	ds_read_b128 v[46:49], v129 offset:42688
	ds_read_b128 v[164:167], v129 offset:42752
	ds_read_b128 v[168:171], v129 offset:49344
	ds_read_b128 v[172:175], v129 offset:49408
	s_waitcnt lgkmcnt(6)
	v_mfma_f32_16x16x32_f16 v[2:5], v[152:155], v[30:33], v[2:5]
	ds_read_b128 v[152:155], v129 offset:56000
	ds_read_b128 v[176:179], v129 offset:56064
	ds_read_b128 v[180:183], v98 offset:63808
	ds_read_b128 v[184:187], v98 offset:64064
	s_waitcnt lgkmcnt(8)
	v_mfma_f32_16x16x32_f16 v[2:5], v[160:163], v[156:159], v[2:5]
	ds_read_b128 v[160:163], v98 offset:63872
	ds_read_b128 v[188:191], v98 offset:64128
	v_mfma_f32_16x16x32_f16 v[14:17], v[42:45], v[26:29], v[14:17]
	s_waitcnt lgkmcnt(2)
	s_nop 3
	v_pk_fma_f32 v[2:3], v[2:3], v[180:181], v[184:185]
	s_nop 0
	v_pk_mul_f32 v[26:27], v[2:3], s[28:29] op_sel_hi:[1,0]
	v_mfma_f32_16x16x32_f16 v[6:9], v[34:37], v[18:21], v[6:9]
	v_mul_f32_e64 v29, |v26|, -|v26|
	v_mul_f32_e32 v29, 0x3fb8aa3b, v29
	v_fma_f32 v28, |v26|, s74, 1.0
	v_exp_f32_e32 v34, v29
	v_fma_f32 v29, |v27|, s74, 1.0
	v_rcp_f32_e32 v28, v28
	v_rcp_f32_e32 v29, v29
	v_mfma_f32_16x16x32_f16 v[10:13], v[54:57], v[18:21], v[10:13]
	v_mul_f32_e64 v35, |v27|, -|v27|
	v_mul_f32_e32 v35, 0x3fb8aa3b, v35
	v_exp_f32_e32 v35, v35
	v_mfma_f32_16x16x32_f16 v[16:19], v[38:41], v[18:21], v[14:17]
	v_mul_f32_e64 v2, v2, 0.5
	v_mul_f32_e64 v3, v3, 0.5
	s_nop 0
	v_mov_b64_e32 v[14:15], s[34:35]
	v_pk_fma_f32 v[20:21], v[28:29], s[40:41], v[14:15] op_sel_hi:[1,0,0]
	v_mfma_f32_16x16x32_f16 v[10:13], v[58:61], v[22:25], v[10:13]
	v_fma_f32 v20, v28, v20, s42
	v_fma_f32 v21, v29, v21, s42
	v_pk_fma_f32 v[20:21], v[28:29], v[20:21], s[44:45] op_sel_hi:[1,1,0]
	v_mfma_f32_16x16x32_f16 v[6:9], v[50:53], v[22:25], v[6:9]
	v_fma_f32 v20, v28, v20, s46
	v_fma_f32 v21, v29, v21, s46
	v_pk_mul_f32 v[20:21], v[20:21], v[28:29] neg_lo:[0,1] neg_hi:[0,1]
	v_mfma_f32_16x16x32_f16 v[16:19], v[62:65], v[22:25], v[16:19]
	v_fma_f32 v20, v20, v34, 1.0
	v_fma_f32 v21, v21, v35, 1.0
	v_bfi_b32 v21, s71, v21, v27
	v_bfi_b32 v20, s71, v20, v26
	v_pk_fma_f32 v[26:27], v[4:5], v[182:183], v[186:187]
	v_pk_add_f32 v[20:21], v[20:21], 1.0 op_sel_hi:[1,0]
	v_pk_mul_f32 v[28:29], v[26:27], s[28:29] op_sel_hi:[1,0]
	v_pk_mul_f32 v[24:25], v[2:3], v[20:21]
	v_mfma_f32_16x16x32_f16 v[2:5], v[168:171], v[30:33], v[10:13]
	v_mul_f32_e64 v26, v26, 0.5
	v_mul_f32_e64 v27, v27, 0.5
	s_nop 0
	v_fma_f32 v10, |v28|, s74, 1.0
	v_fma_f32 v11, |v29|, s74, 1.0
	v_rcp_f32_e32 v34, v10
	v_rcp_f32_e32 v35, v11
	v_mul_f32_e64 v10, |v28|, -|v28|
	v_mul_f32_e32 v10, 0x3fb8aa3b, v10
	v_mfma_f32_16x16x32_f16 v[6:9], v[46:49], v[30:33], v[6:9]
	v_mfma_f32_16x16x32_f16 v[16:19], v[152:155], v[30:33], v[16:19]
	v_exp_f32_e32 v30, v10
	v_mfma_f32_16x16x32_f16 v[10:13], v[172:175], v[156:159], v[2:5]
	s_nop 2
	v_mul_f32_e64 v4, |v29|, -|v29|
	v_pk_fma_f32 v[2:3], v[34:35], s[40:41], v[14:15] op_sel_hi:[1,0,0]
	v_mul_f32_e32 v4, 0x3fb8aa3b, v4
	v_pk_fma_f32 v[2:3], v[34:35], v[2:3], s[42:43] op_sel_hi:[1,1,0]
	v_exp_f32_e32 v31, v4
	v_pk_fma_f32 v[2:3], v[34:35], v[2:3], s[44:45] op_sel_hi:[1,1,0]
	v_mfma_f32_16x16x32_f16 v[20:23], v[164:167], v[156:159], v[6:9]
	v_fma_f32 v2, v34, v2, s46
	v_fma_f32 v3, v35, v3, s46
	v_pk_mul_f32 v[2:3], v[2:3], v[34:35] neg_lo:[0,1] neg_hi:[0,1]
	v_mfma_f32_16x16x32_f16 v[6:9], v[176:179], v[156:159], v[16:19]
	v_fma_f32 v2, v2, v30, 1.0
	v_fma_f32 v3, v3, v31, 1.0
	v_bfi_b32 v3, s71, v3, v29
	v_bfi_b32 v2, s71, v2, v28
	v_pk_add_f32 v[2:3], v[2:3], 1.0 op_sel_hi:[1,0]
	s_nop 0
	v_pk_mul_f32 v[4:5], v[26:27], v[2:3]
	v_cvt_pk_f16_f32 v2, v24, v25
	v_cvt_pk_f16_f32 v3, v4, v5
	s_waitcnt lgkmcnt(0)
	v_pk_fma_f32 v[4:5], v[20:21], v[160:161], v[188:189]
	s_nop 0
	v_pk_mul_f32 v[16:17], v[4:5], s[28:29] op_sel_hi:[1,0]
	v_pk_mul_f32 v[4:5], v[4:5], 0.5 op_sel_hi:[1,0]
	v_fma_f32 v18, |v16|, s74, 1.0
	v_fma_f32 v19, |v17|, s74, 1.0
	v_rcp_f32_e32 v18, v18
	v_rcp_f32_e32 v19, v19
	v_mul_f32_e64 v20, |v16|, -|v16|
	v_mul_f32_e64 v21, |v17|, -|v17|
	v_mul_f32_e32 v20, 0x3fb8aa3b, v20
	v_pk_fma_f32 v[24:25], v[18:19], s[40:41], v[14:15] op_sel_hi:[1,0,0]
	v_mul_f32_e32 v21, 0x3fb8aa3b, v21
	v_exp_f32_e32 v20, v20
	v_pk_fma_f32 v[24:25], v[18:19], v[24:25], s[42:43] op_sel_hi:[1,1,0]
	v_exp_f32_e32 v21, v21
	v_pk_fma_f32 v[24:25], v[18:19], v[24:25], s[44:45] op_sel_hi:[1,1,0]
	s_nop 0
	v_pk_fma_f32 v[24:25], v[18:19], v[24:25], s[46:47] op_sel_hi:[1,1,0]
	s_nop 0
	v_pk_mul_f32 v[18:19], v[24:25], v[18:19] neg_lo:[0,1] neg_hi:[0,1]
	s_nop 0
	v_pk_fma_f32 v[18:19], v[18:19], v[20:21], 1.0 op_sel_hi:[1,1,0]
	s_nop 0
	v_bfi_b32 v17, s71, v19, v17
	v_bfi_b32 v16, s71, v18, v16
	v_pk_add_f32 v[16:17], v[16:17], 1.0 op_sel_hi:[1,0]
	s_nop 0
	v_pk_mul_f32 v[4:5], v[4:5], v[16:17]
	v_pk_fma_f32 v[16:17], v[22:23], v[162:163], v[190:191]
	v_cvt_pk_f16_f32 v4, v4, v5
	v_pk_mul_f32 v[18:19], v[16:17], s[28:29] op_sel_hi:[1,0]
	v_pk_mul_f32 v[16:17], v[16:17], 0.5 op_sel_hi:[1,0]
	v_fma_f32 v20, |v18|, s74, 1.0
	v_fma_f32 v21, |v19|, s74, 1.0
	v_rcp_f32_e32 v20, v20
	v_rcp_f32_e32 v21, v21
	v_mul_f32_e64 v22, |v18|, -|v18|
	v_mul_f32_e64 v23, |v19|, -|v19|
	v_mul_f32_e32 v22, 0x3fb8aa3b, v22
	v_pk_fma_f32 v[24:25], v[20:21], s[40:41], v[14:15] op_sel_hi:[1,0,0]
	v_mul_f32_e32 v23, 0x3fb8aa3b, v23
	v_exp_f32_e32 v22, v22
	v_pk_fma_f32 v[24:25], v[20:21], v[24:25], s[42:43] op_sel_hi:[1,1,0]
	v_exp_f32_e32 v23, v23
	v_pk_fma_f32 v[24:25], v[20:21], v[24:25], s[44:45] op_sel_hi:[1,1,0]
	s_nop 0
	v_pk_fma_f32 v[24:25], v[20:21], v[24:25], s[46:47] op_sel_hi:[1,1,0]
	s_nop 0
	v_pk_mul_f32 v[20:21], v[24:25], v[20:21] neg_lo:[0,1] neg_hi:[0,1]
	s_nop 0
	v_pk_fma_f32 v[20:21], v[20:21], v[22:23], 1.0 op_sel_hi:[1,1,0]
	s_nop 0
	v_bfi_b32 v19, s71, v21, v19
	v_bfi_b32 v18, s71, v20, v18
	v_pk_add_f32 v[18:19], v[18:19], 1.0 op_sel_hi:[1,0]
	s_nop 0
	v_pk_mul_f32 v[16:17], v[16:17], v[18:19]
	ds_read_b128 v[18:21], v98 offset:63936
	ds_read_b128 v[22:25], v98 offset:64192
	v_cvt_pk_f16_f32 v5, v16, v17
	ds_read_b128 v[26:29], v98 offset:64000
	ds_read_b128 v[30:33], v98 offset:64256
	s_waitcnt lgkmcnt(2)
	v_pk_fma_f32 v[10:11], v[10:11], v[18:19], v[22:23]
	s_nop 0
	v_pk_mul_f32 v[22:23], v[10:11], s[28:29] op_sel_hi:[1,0]
	v_pk_fma_f32 v[12:13], v[12:13], v[20:21], v[24:25]
	v_fma_f32 v16, |v22|, s74, 1.0
	v_fma_f32 v17, |v23|, s74, 1.0
	v_rcp_f32_e32 v16, v16
	v_rcp_f32_e32 v17, v17
	v_mul_f32_e64 v18, |v22|, -|v22|
	v_mul_f32_e64 v19, |v23|, -|v23|
	v_mul_f32_e32 v18, 0x3fb8aa3b, v18
	v_pk_fma_f32 v[34:35], v[16:17], s[40:41], v[14:15] op_sel_hi:[1,0,0]
	v_mul_f32_e32 v19, 0x3fb8aa3b, v19
	v_exp_f32_e32 v18, v18
	v_pk_fma_f32 v[34:35], v[16:17], v[34:35], s[42:43] op_sel_hi:[1,1,0]
	v_exp_f32_e32 v19, v19
	v_pk_fma_f32 v[34:35], v[16:17], v[34:35], s[44:45] op_sel_hi:[1,1,0]
	v_pk_mul_f32 v[10:11], v[10:11], 0.5 op_sel_hi:[1,0]
	v_pk_fma_f32 v[34:35], v[16:17], v[34:35], s[46:47] op_sel_hi:[1,1,0]
	v_pk_mul_f32 v[20:21], v[12:13], s[28:29] op_sel_hi:[1,0]
	v_pk_mul_f32 v[16:17], v[34:35], v[16:17] neg_lo:[0,1] neg_hi:[0,1]
	v_mul_f32_e64 v24, |v20|, -|v20|
	v_pk_fma_f32 v[46:47], v[16:17], v[18:19], 1.0 op_sel_hi:[1,1,0]
	v_lshl_add_u64 v[18:19], s[50:51], 1, v[100:101]
	global_load_dwordx4 v[34:37], v[18:19], off
	global_load_dwordx4 v[42:45], v[18:19], off offset:1024
	v_lshl_add_u64 v[16:17], s[50:51], 2, v[102:103]
	global_load_dwordx4 v[38:41], v[16:17], off
	v_mov_b32_e32 v190, 0x1000
	v_mov_b32_e32 v191, 0
	global_load_dwordx4 v[152:155], v[18:19], off offset:2048
	global_load_dwordx4 v[156:159], v[18:19], off offset:3072
	global_load_dwordx4 v[160:163], v[16:17], off offset:64
	v_lshl_add_u64 v[188:189], v[18:19], 0, v[190:191]
	global_load_dwordx4 v[164:167], v[188:189], off
	global_load_dwordx4 v[168:171], v[188:189], off offset:1024
	global_load_dwordx4 v[172:175], v[16:17], off offset:128
	global_load_dwordx4 v[176:179], v[188:189], off offset:2048
	global_load_dwordx4 v[180:183], v[188:189], off offset:3072
	global_load_dwordx4 v[184:187], v[16:17], off offset:192
	v_bfi_b32 v23, s71, v47, v23
	v_bfi_b32 v22, s71, v46, v22
	v_pk_add_f32 v[22:23], v[22:23], 1.0 op_sel_hi:[1,0]
	v_mul_f32_e64 v25, |v21|, -|v21|
	v_pk_mul_f32 v[10:11], v[10:11], v[22:23]
	v_fma_f32 v22, |v20|, s74, 1.0
	v_fma_f32 v23, |v21|, s74, 1.0
	v_rcp_f32_e32 v22, v22
	v_rcp_f32_e32 v23, v23
	v_mul_f32_e32 v24, 0x3fb8aa3b, v24
	v_mul_f32_e32 v25, 0x3fb8aa3b, v25
	v_exp_f32_e32 v24, v24
	v_pk_fma_f32 v[46:47], v[22:23], s[40:41], v[14:15] op_sel_hi:[1,0,0]
	v_exp_f32_e32 v25, v25
	v_pk_fma_f32 v[46:47], v[22:23], v[46:47], s[42:43] op_sel_hi:[1,1,0]
	v_pk_mul_f32 v[12:13], v[12:13], 0.5 op_sel_hi:[1,0]
	v_pk_fma_f32 v[46:47], v[22:23], v[46:47], s[44:45] op_sel_hi:[1,1,0]
	s_waitcnt lgkmcnt(0)
	v_pk_fma_f32 v[6:7], v[6:7], v[26:27], v[30:31]
	v_pk_fma_f32 v[46:47], v[22:23], v[46:47], s[46:47] op_sel_hi:[1,1,0]
	v_cvt_pk_f16_f32 v10, v10, v11
	v_pk_mul_f32 v[22:23], v[46:47], v[22:23] neg_lo:[0,1] neg_hi:[0,1]
	v_pk_fma_f32 v[8:9], v[8:9], v[28:29], v[32:33]
	v_pk_fma_f32 v[22:23], v[22:23], v[24:25], 1.0 op_sel_hi:[1,1,0]
	s_mul_i32 s50, s94, 0xfef85000
	v_bfi_b32 v21, s71, v23, v21
	v_bfi_b32 v20, s71, v22, v20
	v_pk_add_f32 v[20:21], v[20:21], 1.0 op_sel_hi:[1,0]
	s_nop 0
	v_pk_mul_f32 v[12:13], v[12:13], v[20:21]
	s_nop 0
	v_cvt_pk_f16_f32 v11, v12, v13
	v_pk_mul_f32 v[12:13], v[6:7], s[28:29] op_sel_hi:[1,0]
	v_pk_mul_f32 v[6:7], v[6:7], 0.5 op_sel_hi:[1,0]
	v_fma_f32 v20, |v12|, s74, 1.0
	v_fma_f32 v21, |v13|, s74, 1.0
	v_rcp_f32_e32 v20, v20
	v_rcp_f32_e32 v21, v21
	v_mul_f32_e64 v22, |v12|, -|v12|
	v_mul_f32_e64 v23, |v13|, -|v13|
	v_mul_f32_e32 v22, 0x3fb8aa3b, v22
	v_pk_fma_f32 v[24:25], v[20:21], s[40:41], v[14:15] op_sel_hi:[1,0,0]
	v_mul_f32_e32 v23, 0x3fb8aa3b, v23
	v_exp_f32_e32 v22, v22
	v_pk_fma_f32 v[24:25], v[20:21], v[24:25], s[42:43] op_sel_hi:[1,1,0]
	v_exp_f32_e32 v23, v23
	v_pk_fma_f32 v[24:25], v[20:21], v[24:25], s[44:45] op_sel_hi:[1,1,0]
	s_nop 0
	v_pk_fma_f32 v[24:25], v[20:21], v[24:25], s[46:47] op_sel_hi:[1,1,0]
	s_nop 0
	v_pk_mul_f32 v[20:21], v[24:25], v[20:21] neg_lo:[0,1] neg_hi:[0,1]
	s_nop 0
	v_pk_fma_f32 v[20:21], v[20:21], v[22:23], 1.0 op_sel_hi:[1,1,0]
	s_nop 0
	v_bfi_b32 v13, s71, v21, v13
	v_bfi_b32 v12, s71, v20, v12
	v_pk_add_f32 v[12:13], v[12:13], 1.0 op_sel_hi:[1,0]
	s_nop 0
	v_pk_mul_f32 v[6:7], v[6:7], v[12:13]
	v_pk_mul_f32 v[12:13], v[8:9], s[28:29] op_sel_hi:[1,0]
	v_pk_mul_f32 v[8:9], v[8:9], 0.5 op_sel_hi:[1,0]
	v_fma_f32 v20, |v12|, s74, 1.0
	v_fma_f32 v21, |v13|, s74, 1.0
	v_rcp_f32_e32 v20, v20
	v_rcp_f32_e32 v21, v21
	v_mul_f32_e64 v22, |v12|, -|v12|
	v_mul_f32_e64 v23, |v13|, -|v13|
	v_mul_f32_e32 v22, 0x3fb8aa3b, v22
	v_pk_fma_f32 v[14:15], v[20:21], s[40:41], v[14:15] op_sel_hi:[1,0,0]
	v_mul_f32_e32 v23, 0x3fb8aa3b, v23
	v_exp_f32_e32 v22, v22
	v_pk_fma_f32 v[14:15], v[20:21], v[14:15], s[42:43] op_sel_hi:[1,1,0]
	v_exp_f32_e32 v23, v23
	v_pk_fma_f32 v[14:15], v[20:21], v[14:15], s[44:45] op_sel_hi:[1,1,0]
	s_nop 0
	v_pk_fma_f32 v[14:15], v[20:21], v[14:15], s[46:47] op_sel_hi:[1,1,0]
	s_nop 0
	v_pk_mul_f32 v[14:15], v[14:15], v[20:21] neg_lo:[0,1] neg_hi:[0,1]
	s_nop 0
	v_pk_fma_f32 v[14:15], v[14:15], v[22:23], 1.0 op_sel_hi:[1,1,0]
	s_nop 0
	v_bfi_b32 v13, s71, v15, v13
	v_bfi_b32 v12, s71, v14, v12
	v_pk_add_f32 v[12:13], v[12:13], 1.0 op_sel_hi:[1,0]
	v_add_u32_e32 v14, s95, v128
	v_pk_mul_f32 v[8:9], v[8:9], v[12:13]
	v_cvt_pk_f16_f32 v12, v6, v7
	v_cvt_pk_f16_f32 v13, v8, v9
	s_waitcnt vmcnt(0)
	v_pk_mul_f32 v[8:9], v[40:41], s[48:49] op_sel_hi:[1,0]
	v_pk_mul_f32 v[6:7], v[38:39], s[48:49] op_sel_hi:[1,0]
	v_cmp_gt_i32_e64 s[20:21], s73, v14
	v_add_u32_e32 v14, s50, v134
	v_mfma_f32_16x16x32_f16 v[6:9], v[34:37], v[2:5], v[6:9]
	v_mfma_f32_16x16x32_f16 v[6:9], v[42:45], v[10:13], v[6:9]
	v_pk_mul_f32 v[160:161], v[160:161], s[48:49] op_sel_hi:[1,0]
	v_pk_mul_f32 v[162:163], v[162:163], s[48:49] op_sel_hi:[1,0]
	v_pk_mul_f32 v[172:173], v[172:173], s[48:49] op_sel_hi:[1,0]
	v_pk_mul_f32 v[174:175], v[174:175], s[48:49] op_sel_hi:[1,0]
	v_pk_mul_f32 v[184:185], v[184:185], s[48:49] op_sel_hi:[1,0]
	v_pk_mul_f32 v[186:187], v[186:187], s[48:49] op_sel_hi:[1,0]
	s_nop 1
	v_mfma_f32_16x16x32_f16 v[20:23], v[152:155], v[2:5], v[160:163]
	v_mfma_f32_16x16x32_f16 v[24:27], v[164:167], v[2:5], v[172:175]
	v_mfma_f32_16x16x32_f16 v[28:31], v[176:179], v[2:5], v[184:187]
	v_mfma_f32_16x16x32_f16 v[20:23], v[156:159], v[10:13], v[20:23]
	v_mfma_f32_16x16x32_f16 v[24:27], v[168:171], v[10:13], v[24:27]
	v_mfma_f32_16x16x32_f16 v[28:31], v[180:183], v[10:13], v[28:31]
	s_and_saveexec_b64 s[50:51], s[20:21]
	s_cbranch_execz .Lmy_k2_nostore
	s_nop 7
	buffer_store_dwordx4 v[6:9], v14, s[24:27], 0 offen sc1
	buffer_store_dwordx4 v[20:23], v14, s[24:27], 0 offen offset:64 sc1
	buffer_store_dwordx4 v[24:27], v14, s[24:27], 0 offen offset:128 sc1
	buffer_store_dwordx4 v[28:31], v14, s[24:27], 0 offen offset:192 sc1

	.amdhsa_kernel _Z10k_enc_scanPKDF16_PKfS2_S2_S2_S2_S2_S2_S2_S2_S2_S0_S2_S2_S2_S2_S2_S0_S2_PfPjS2_S2_S2_S2_S2_S2_S2_S2_S2_S2_S2_S2_PDF16_S5_S3_
		.amdhsa_group_segment_fixed_size 91136
		.amdhsa_private_segment_fixed_size 0
		.amdhsa_kernarg_size 288
		.amdhsa_user_sgpr_count 2
		.amdhsa_user_sgpr_dispatch_ptr 0
		.amdhsa_user_sgpr_queue_ptr 0
		.amdhsa_user_sgpr_kernarg_segment_ptr 1
		.amdhsa_user_sgpr_dispatch_id 0
		.amdhsa_user_sgpr_kernarg_preload_length 0
		.amdhsa_user_sgpr_kernarg_preload_offset 0
		.amdhsa_user_sgpr_private_segment_size 0
		.amdhsa_uses_dynamic_stack 0
		.amdhsa_enable_private_segment 0
		.amdhsa_system_sgpr_workgroup_id_x 1
		.amdhsa_system_sgpr_workgroup_id_y 0
		.amdhsa_system_sgpr_workgroup_id_z 0
		.amdhsa_system_sgpr_workgroup_info 0
		.amdhsa_system_vgpr_workitem_id 0
		.amdhsa_next_free_vgpr 250
		.amdhsa_next_free_sgpr 100
		.amdhsa_accum_offset 252
		.amdhsa_reserve_vcc 1
		.amdhsa_float_round_mode_32 0
		.amdhsa_float_round_mode_16_64 0
		.amdhsa_float_denorm_mode_32 3
		.amdhsa_float_denorm_mode_16_64 3
		.amdhsa_dx10_clamp 1
		.amdhsa_ieee_mode 1
		.amdhsa_fp16_overflow 0
		.amdhsa_tg_split 0
		.amdhsa_exception_fp_ieee_invalid_op 0
		.amdhsa_exception_fp_denorm_src 0
		.amdhsa_exception_fp_ieee_div_zero 0
		.amdhsa_exception_fp_ieee_overflow 0
		.amdhsa_exception_fp_ieee_underflow 0
		.amdhsa_exception_fp_ieee_inexact 0
		.amdhsa_exception_int_div_zero 0
	.end_amdhsa_kernel

amdhsa.kernels:
  - .agpr_count:     8
    .args:
      - .actual_access:  read_only
        .address_space:  global
        .offset:         0
        .size:           8
        .value_kind:     global_buffer
      - .actual_access:  read_only
        .address_space:  global
        .offset:         8
        .size:           8
        .value_kind:     global_buffer
      - .actual_access:  write_only
        .address_space:  global
        .offset:         16
        .size:           8
        .value_kind:     global_buffer
      - .actual_access:  write_only
        .address_space:  global
        .offset:         24
        .size:           8
        .value_kind:     global_buffer
      - .actual_access:  read_only
        .address_space:  global
        .offset:         32
        .size:           8
        .value_kind:     global_buffer
      - .actual_access:  read_only
        .address_space:  global
        .offset:         40
        .size:           8
        .value_kind:     global_buffer
      - .actual_access:  write_only
        .address_space:  global
        .offset:         48
        .size:           8
        .value_kind:     global_buffer
      - .actual_access:  write_only
        .address_space:  global
        .offset:         56
        .size:           8
        .value_kind:     global_buffer
      - .actual_access:  write_only
        .address_space:  global
        .offset:         64
        .size:           8
        .value_kind:     global_buffer
    .group_segment_fixed_size: 24976
    .kernarg_segment_align: 8
    .kernarg_segment_size: 72
    .language:       OpenCL C
    .language_version:
      - 2
      - 0
    .max_flat_workgroup_size: 256
    .name:           _Z9k_fb_mfmaPKfS0_PDF16_PfS0_S0_S1_S1_Pj
    .private_segment_fixed_size: 0
    .sgpr_count:     24
    .sgpr_spill_count: 0
    .symbol:         _Z9k_fb_mfmaPKfS0_PDF16_PfS0_S0_S1_S1_Pj.kd
    .uniform_work_group_size: 1
    .uses_dynamic_stack: false
    .vgpr_count:     92
    .vgpr_spill_count: 0
    .wavefront_size: 64
  - .agpr_count:     0
    .args:
      - .actual_access:  read_only
        .address_space:  global
        .offset:         0
        .size:           8
        .value_kind:     global_buffer
      - .actual_access:  read_only
        .address_space:  global
        .offset:         8
        .size:           8
        .value_kind:     global_buffer
      - .actual_access:  write_only
        .address_space:  global
        .offset:         16
        .size:           8
        .value_kind:     global_buffer
      - .actual_access:  write_only
        .address_space:  global
        .offset:         24
        .size:           8
        .value_kind:     global_buffer
    .group_segment_fixed_size: 0
    .kernarg_segment_align: 8
    .kernarg_segment_size: 32
    .language:       OpenCL C
    .language_version:
      - 2
      - 0
    .max_flat_workgroup_size: 1024
    .name:           _Z6k_prepPKfS0_PDF16_S1_
    .private_segment_fixed_size: 0
    .sgpr_count:     19
    .sgpr_spill_count: 0
    .symbol:         _Z6k_prepPKfS0_PDF16_S1_.kd
    .uniform_work_group_size: 1
    .uses_dynamic_stack: false
    .vgpr_count:     8
    .vgpr_spill_count: 0
    .wavefront_size: 64
  - .agpr_count:     0
    .args:
      - .actual_access:  read_only
        .address_space:  global
        .offset:         0
        .size:           8
        .value_kind:     global_buffer
      - .actual_access:  read_only
        .address_space:  global
        .offset:         8
        .size:           8
        .value_kind:     global_buffer
      - .actual_access:  read_only
        .address_space:  global
        .offset:         16
        .size:           8
        .value_kind:     global_buffer
      - .actual_access:  read_only
        .address_space:  global
        .offset:         24
        .size:           8
        .value_kind:     global_buffer
      - .actual_access:  read_only
        .address_space:  global
        .offset:         32
        .size:           8
        .value_kind:     global_buffer
      - .actual_access:  read_only
        .address_space:  global
        .offset:         40
        .size:           8
        .value_kind:     global_buffer
      - .actual_access:  read_only
        .address_space:  global
        .offset:         48
        .size:           8
        .value_kind:     global_buffer
      - .actual_access:  read_only
        .address_space:  global
        .offset:         56
        .size:           8
        .value_kind:     global_buffer
      - .actual_access:  read_only
        .address_space:  global
        .offset:         64
        .size:           8
        .value_kind:     global_buffer
      - .actual_access:  read_only
        .address_space:  global
        .offset:         72
        .size:           8
        .value_kind:     global_buffer
      - .actual_access:  write_only
        .address_space:  global
        .offset:         80
        .size:           8
        .value_kind:     global_buffer
      - .actual_access:  write_only
        .address_space:  global
        .offset:         88
        .size:           8
        .value_kind:     global_buffer
    .group_segment_fixed_size: 236
    .kernarg_segment_align: 8
    .kernarg_segment_size: 96
    .language:       OpenCL C
    .language_version:
      - 2
      - 0
    .max_flat_workgroup_size: 192
    .name:           _Z6k_gatePKfS0_S0_S0_S0_S0_S0_S0_S0_S0_PfPj
    .private_segment_fixed_size: 0
    .sgpr_count:     32
    .sgpr_spill_count: 0
    .symbol:         _Z6k_gatePKfS0_S0_S0_S0_S0_S0_S0_S0_S0_PfPj.kd
    .uniform_work_group_size: 1
    .uses_dynamic_stack: false
    .vgpr_count:     47
    .vgpr_spill_count: 0
    .wavefront_size: 64
  - .agpr_count:     0
    .args:
      - .actual_access:  read_only
        .address_space:  global
        .offset:         0
        .size:           8
        .value_kind:     global_buffer
      - .actual_access:  read_only
        .address_space:  global
        .offset:         8
        .size:           8
        .value_kind:     global_buffer
      - .actual_access:  read_only
        .address_space:  global
        .offset:         16
        .size:           8
        .value_kind:     global_buffer
      - .actual_access:  read_only
        .address_space:  global
        .offset:         24
        .size:           8
        .value_kind:     global_buffer
      - .actual_access:  read_only
        .address_space:  global
        .offset:         32
        .size:           8
        .value_kind:     global_buffer
      - .actual_access:  read_only
        .address_space:  global
        .offset:         40
        .size:           8
        .value_kind:     global_buffer
      - .actual_access:  read_only
        .address_space:  global
        .offset:         48
        .size:           8
        .value_kind:     global_buffer
      - .actual_access:  read_only
        .address_space:  global
        .offset:         56
        .size:           8
        .value_kind:     global_buffer
      - .actual_access:  read_only
        .address_space:  global
        .offset:         64
        .size:           8
        .value_kind:     global_buffer
      - .actual_access:  read_only
        .address_space:  global
        .offset:         72
        .size:           8
        .value_kind:     global_buffer
      - .actual_access:  read_only
        .address_space:  global
        .offset:         80
        .size:           8
        .value_kind:     global_buffer
      - .actual_access:  read_only
        .address_space:  global
        .offset:         88
        .size:           8
        .value_kind:     global_buffer
      - .actual_access:  read_only
        .address_space:  global
        .offset:         96
        .size:           8
        .value_kind:     global_buffer
      - .actual_access:  read_only
        .address_space:  global
        .offset:         104
        .size:           8
        .value_kind:     global_buffer
      - .actual_access:  read_only
        .address_space:  global
        .offset:         112
        .size:           8
        .value_kind:     global_buffer
      - .actual_access:  read_only
        .address_space:  global
        .offset:         120
        .size:           8
        .value_kind:     global_buffer
      - .actual_access:  read_only
        .address_space:  global
        .offset:         128
        .size:           8
        .value_kind:     global_buffer
      - .actual_access:  read_only
        .address_space:  global
        .offset:         136
        .size:           8
        .value_kind:     global_buffer
      - .actual_access:  read_only
        .address_space:  global
        .offset:         144
        .size:           8
        .value_kind:     global_buffer
      - .address_space:  global
        .offset:         152
        .size:           8
        .value_kind:     global_buffer
      - .address_space:  global
        .offset:         160
        .size:           8
        .value_kind:     global_buffer
      - .actual_access:  read_only
        .address_space:  global
        .offset:         168
        .size:           8
        .value_kind:     global_buffer
      - .actual_access:  read_only
        .address_space:  global
        .offset:         176
        .size:           8
        .value_kind:     global_buffer
      - .actual_access:  read_only
        .address_space:  global
        .offset:         184
        .size:           8
        .value_kind:     global_buffer
      - .actual_access:  read_only
        .address_space:  global
        .offset:         192
        .size:           8
        .value_kind:     global_buffer
      - .actual_access:  read_only
        .address_space:  global
        .offset:         200
        .size:           8
        .value_kind:     global_buffer
      - .actual_access:  read_only
        .address_space:  global
        .offset:         208
        .size:           8
        .value_kind:     global_buffer
      - .actual_access:  read_only
        .address_space:  global
        .offset:         216
        .size:           8
        .value_kind:     global_buffer
      - .actual_access:  read_only
        .address_space:  global
        .offset:         224
        .size:           8
        .value_kind:     global_buffer
      - .actual_access:  read_only
        .address_space:  global
        .offset:         232
        .size:           8
        .value_kind:     global_buffer
      - .actual_access:  read_only
        .address_space:  global
        .offset:         240
        .size:           8
        .value_kind:     global_buffer
      - .actual_access:  read_only
        .address_space:  global
        .offset:         248
        .size:           8
        .value_kind:     global_buffer
      - .actual_access:  read_only
        .address_space:  global
        .offset:         256
        .size:           8
        .value_kind:     global_buffer
      - .actual_access:  write_only
        .address_space:  global
        .offset:         264
        .size:           8
        .value_kind:     global_buffer
      - .actual_access:  write_only
        .address_space:  global
        .offset:         272
        .size:           8
        .value_kind:     global_buffer
      - .actual_access:  write_only
        .address_space:  global
        .offset:         280
        .size:           8
        .value_kind:     global_buffer
    .group_segment_fixed_size: 91136
    .kernarg_segment_align: 8
    .kernarg_segment_size: 288
    .language:       OpenCL C
    .language_version:
      - 2
      - 0
    .max_flat_workgroup_size: 320
    .name:           _Z10k_enc_scanPKDF16_PKfS2_S2_S2_S2_S2_S2_S2_S2_S2_S0_S2_S2_S2_S2_S2_S0_S2_PfPjS2_S2_S2_S2_S2_S2_S2_S2_S2_S2_S2_S2_PDF16_S5_S3_
    .private_segment_fixed_size: 0
    .sgpr_count:     106
    .sgpr_spill_count: 0
    .symbol:         _Z10k_enc_scanPKDF16_PKfS2_S2_S2_S2_S2_S2_S2_S2_S2_S0_S2_S2_S2_S2_S2_S0_S2_PfPjS2_S2_S2_S2_S2_S2_S2_S2_S2_S2_S2_S2_PDF16_S5_S3_.kd
    .uniform_work_group_size: 1
    .uses_dynamic_stack: false
    .vgpr_count:     250
    .vgpr_spill_count: 0
    .wavefront_size: 64
  - .agpr_count:     0
    .args:
      - .actual_access:  read_only
        .address_space:  global
        .offset:         0
        .size:           8
        .value_kind:     global_buffer
      - .actual_access:  read_only
        .address_space:  global
        .offset:         8
        .size:           8
        .value_kind:     global_buffer
      - .actual_access:  write_only
        .address_space:  global
        .offset:         16
        .size:           8
        .value_kind:     global_buffer
    .group_segment_fixed_size: 66580
    .kernarg_segment_align: 8
    .kernarg_segment_size: 24
    .language:       OpenCL C
    .language_version:
      - 2
      - 0
    .max_flat_workgroup_size: 320
    .name:           _Z7k_att1nPKDF16_S0_Pf
    .private_segment_fixed_size: 0
    .sgpr_count:     29
    .sgpr_spill_count: 0
    .symbol:         _Z7k_att1nPKDF16_S0_Pf.kd
    .uniform_work_group_size: 1
    .uses_dynamic_stack: false
    .vgpr_count:     126
    .vgpr_spill_count: 0
    .wavefront_size: 64
  - .agpr_count:     0
    .args:
      - .actual_access:  read_only
        .address_space:  global
        .offset:         0
        .size:           8
        .value_kind:     global_buffer
      - .actual_access:  read_only
        .address_space:  global
        .offset:         8
        .size:           8
        .value_kind:     global_buffer
      - .actual_access:  read_only
        .address_space:  global
        .offset:         16
        .size:           8
        .value_kind:     global_buffer
      - .actual_access:  write_only
        .address_space:  global
        .offset:         24
        .size:           8
        .value_kind:     global_buffer
      - .actual_access:  read_only
        .address_space:  global
        .offset:         32
        .size:           8
        .value_kind:     global_buffer
      - .actual_access:  read_only
        .address_space:  global
        .offset:         40
        .size:           8
        .value_kind:     global_buffer
      - .actual_access:  read_only
        .address_space:  global
        .offset:         48
        .size:           8
        .value_kind:     global_buffer
      - .actual_access:  read_only
        .address_space:  global
        .offset:         56
        .size:           8
        .value_kind:     global_buffer
      - .actual_access:  read_only
        .address_space:  global
        .offset:         64
        .size:           8
        .value_kind:     global_buffer
      - .actual_access:  read_only
        .address_space:  global
        .offset:         72
        .size:           8
        .value_kind:     global_buffer
      - .actual_access:  read_only
        .address_space:  global
        .offset:         80
        .size:           8
        .value_kind:     global_buffer
      - .actual_access:  read_only
        .address_space:  global
        .offset:         88
        .size:           8
        .value_kind:     global_buffer
      - .actual_access:  read_only
        .address_space:  global
        .offset:         96
        .size:           8
        .value_kind:     global_buffer
      - .actual_access:  write_only
        .address_space:  global
        .offset:         104
        .size:           8
        .value_kind:     global_buffer
    .group_segment_fixed_size: 70720
    .kernarg_segment_align: 8
    .kernarg_segment_size: 112
    .language:       OpenCL C
    .language_version:
      - 2
      - 0
    .max_flat_workgroup_size: 320
    .name:           _Z7k_att2nPKDF16_S0_PKfPfS2_S2_S2_S2_S2_S2_S2_S2_S2_S3_
    .private_segment_fixed_size: 0
    .sgpr_count:     58
    .sgpr_spill_count: 0
    .symbol:         _Z7k_att2nPKDF16_S0_PKfPfS2_S2_S2_S2_S2_S2_S2_S2_S2_S3_.kd
    .uniform_work_group_size: 1
    .uses_dynamic_stack: false
    .vgpr_count:     122
    .vgpr_spill_count: 0
    .wavefront_size: 64
  - .agpr_count:     0
    .args:
      - .actual_access:  read_only
        .address_space:  global
        .offset:         0
        .size:           8
        .value_kind:     global_buffer
      - .actual_access:  read_only
        .address_space:  global
        .offset:         8
        .size:           8
        .value_kind:     global_buffer
      - .actual_access:  read_only
        .address_space:  global
        .offset:         16
        .size:           8
        .value_kind:     global_buffer
      - .actual_access:  read_only
        .address_space:  global
        .offset:         24
        .size:           8
        .value_kind:     global_buffer
      - .actual_access:  read_only
        .address_space:  global
        .offset:         32
        .size:           8
        .value_kind:     global_buffer
      - .actual_access:  read_only
        .address_space:  global
        .offset:         40
        .size:           8
        .value_kind:     global_buffer
      - .actual_access:  read_only
        .address_space:  global
        .offset:         48
        .size:           8
        .value_kind:     global_buffer
      - .actual_access:  read_only
        .address_space:  global
        .offset:         56
        .size:           8
        .value_kind:     global_buffer
      - .actual_access:  read_only
        .address_space:  global
        .offset:         64
        .size:           8
        .value_kind:     global_buffer
      - .actual_access:  write_only
        .address_space:  global
        .offset:         72
        .size:           8
        .value_kind:     global_buffer
    .group_segment_fixed_size: 704
    .kernarg_segment_align: 8
    .kernarg_segment_size: 80
    .language:       OpenCL C
    .language_version:
      - 2
      - 0
    .max_flat_workgroup_size: 64
    .name:           _Z8k_heads3PKfS0_S0_S0_S0_S0_S0_S0_S0_Pf
    .private_segment_fixed_size: 0
    .sgpr_count:     24
    .sgpr_spill_count: 0
    .symbol:         _Z8k_heads3PKfS0_S0_S0_S0_S0_S0_S0_S0_Pf.kd
    .uniform_work_group_size: 1
    .uses_dynamic_stack: false
    .vgpr_count:     121
    .vgpr_spill_count: 0
    .wavefront_size: 64
